# combo3: adds down-unit prologue de-serialization and final-phase final_g hoist (no per-chunk load+wait before each store)
# baseline (speedup 1.0000x reference)
; __device__ __forceinline__ int tid_opaque() { int t = threadIdx.x; asm volatile("" : "+v"(t)); return t; }
;     __device__ __forceinline__ void init() {
;         const int tid = tid_opaque(), wid = tid >> 6, lane = tid & 63;
;         wr = wid >> 2; wc = wid & 3; fr = lane & 15; fq = lane >> 4;
;         aR = (wid >> 1) * 16 + (lane >> 2); aC = (wid & 1) * 32 + (((lane & 3) ^ ((lane >> 5) << 1)) * 8);
;         a_w = (unsigned)(wid * 1024 + lane * 16);
;         { const int l32 = lane & 31, kc8 = 2 * (wid >> 1) + (lane >> 5), wc_ = l32 >> 3, bfq = (l32 >> 1) & 3, nlo = l32 & 1; b_p = wid & 1;
;           b_k = kc8 * 8; b_col = wc_ * 64 + b_p * 32 + bfq * 8 + nlo * 4; b_gucol = wc_ * 32 + bfq * 8 + nlo * 4;
;           const int sub = wc_ * 4 + 2 * b_p + nlo;
;           b_w = (unsigned)((sub * 2 + (kc8 >> 2)) * 1024 + (((4 * bfq) * 64 + (kc8 & 3) * 16) ^ ((bfq >> 1) << 5))); b_rot = (unsigned)(nlo * 64); }
;         const unsigned lo = (unsigned)((fr * 64 + fq * 16) ^ ((fr >> 3) << 5));
;         a_r = (unsigned)(wr * 16384) + lo; b_r = 32768u + (unsigned)(wc * 8192) + lo;
; __device__ __forceinline__ void phase_moe_down(const Ptrs& p, LAS unsigned char* lds) {
;     ...
;         GemmT T; T.init();
;         const int* list = (const int*)(p.ws + OFF_LIST) + (size_t)mu.e * NTOK; const int i0 = mu.mt * 256, col0 = mu.nt * 256;
;         const unsigned ao = (unsigned)((T.aR * D + T.aC) * 2), bo = (unsigned)((T.b_k * D + T.b_col) * 4);
;         int pa = -1; float pg = 0.f;
;         { const int t_ = tid_opaque(); if (t_ < 256 && i0 + t_ < mu.cnt) { pa = list[i0 + t_]; pg = gate[pa]; } }
.LBB0_1479:
	v_mov_b32_e32 v3, v0
	v_mov_b32_e32 v4, v0
	s_ashr_i32 s43, s42, 31
	s_lshl_b32 s85, s82, 8
	v_mov_b32_e32 v215, 0
	v_cmp_gt_i32_e32 vcc, s65, v4
	v_mov_b32_e32 v214, -1
	s_and_saveexec_b64 s[0:1], vcc
	s_cbranch_execz .LBB0_1483
	v_add_u32_e32 v4, s85, v4
	v_cmp_gt_i32_e32 vcc, s83, v4
	v_mov_b32_e32 v214, -1
	v_mov_b32_e32 v215, 0
	s_and_saveexec_b64 s[4:5], vcc
	s_cbranch_execz .LBB0_1482
	s_lshl_b64 s[2:3], s[42:43], 15
	s_add_u32 s2, s52, s2
	s_addc_u32 s3, s53, s3
	v_ashrrev_i32_e32 v5, 31, v4
	v_lshl_add_u64 v[4:5], v[4:5], 2, s[2:3]
	global_load_dword v214, v[4:5], off
.LBB0_1482:
	s_or_b64 exec, exec, s[4:5]
.LBB0_1483:
	s_or_b64 exec, exec, s[0:1]
	s_add_i32 s2, s84, s85
	s_ashr_i32 s3, s2, 31
	s_lshl_b32 s0, s81, 8
	s_lshl_b64 s[2:3], s[2:3], 12
	s_add_u32 s36, s20, s2
	v_readlane_b32 s4, v246, 0
	s_addc_u32 s1, s28, s3
	v_readlane_b32 s5, v246, 1
	v_readlane_b32 s6, v246, 2
	v_readlane_b32 s7, v246, 3
	v_readlane_b32 s8, v246, 4
	v_readlane_b32 s9, v246, 5
	s_and_b32 s37, s1, 0xffff
	s_lshl_b64 s[2:3], s[42:43], 24
	v_readlane_b32 s10, v246, 6
	v_readlane_b32 s11, v246, 7
	s_mov_b64 s[4:5], s[8:9]
	s_add_u32 s4, s4, s2
	v_ashrrev_i32_e32 v4, 6, v3
	v_bfe_u32 v11, v3, 1, 2
	s_addc_u32 s5, s5, s3
	s_ashr_i32 s1, s0, 31
	v_ashrrev_i32_e32 v5, 7, v3
	v_and_b32_e32 v6, 1, v4
	v_bfe_u32 v8, v3, 5, 1
	v_bfe_u32 v10, v3, 3, 2
	v_and_b32_e32 v12, 1, v3
	v_lshlrev_b32_e32 v14, 3, v11
	s_lshl_b64 s[2:3], s[0:1], 2
	v_lshlrev_b32_e32 v7, 5, v6
	v_lshl_or_b32 v9, v5, 1, v8
	v_lshl_or_b32 v14, v10, 6, v14
	v_lshlrev_b32_e32 v15, 2, v12
	s_add_u32 s24, s4, s2
	v_lshlrev_b32_e32 v13, 16, v9
	v_or3_b32 v14, v14, v15, v7
	s_addc_u32 s1, s5, s3
	v_lshl_or_b32 v222, v14, 2, v13
	s_and_b32 s25, s1, 0xffff
	s_movk_i32 s1, 0x2000
	buffer_load_dwordx4 v[110:113], v222, s[24:27], 0 offen
	buffer_load_dwordx4 v[114:117], v222, s[24:27], s66 offen
	s_mov_b32 s2, 0x8000
	buffer_load_dwordx4 v[122:125], v222, s[24:27], s1 offen
	buffer_load_dwordx4 v[118:121], v222, s[24:27], s2 offen
	s_movk_i32 s1, 0x4000
	s_mov_b32 s2, 0xa000
	buffer_load_dwordx4 v[126:129], v222, s[24:27], s1 offen
	buffer_load_dwordx4 v[130:133], v222, s[24:27], s2 offen
	s_mov_b32 s1, 0xc000
	s_mov_b32 s2, 0xe000
	buffer_load_dwordx4 v[138:141], v222, s[24:27], s1 offen
	buffer_load_dwordx4 v[142:145], v222, s[24:27], s2 offen
	s_waitcnt vmcnt(8)
	v_cmp_ne_u32_e32 vcc, -1, v214
	s_and_saveexec_b64 vcc, vcc
	v_ashrrev_i32_e32 v17, 31, v214
	v_mov_b32_e32 v16, v214
	v_lshl_add_u64 v[16:17], v[16:17], 2, s[56:57]
	global_load_dword v215, v[16:17], off
	s_or_b64 exec, exec, vcc
	v_lshlrev_b32_e32 v16, 3, v3
	v_and_b32_e32 v13, 63, v3
	v_lshlrev_b32_e32 v8, 4, v8
	v_and_b32_e32 v17, 24, v16
	v_bitop3_b32 v7, v8, v7, v17 bitop3:0xde
	v_lshlrev_b32_e32 v8, 4, v13
	v_lshl_or_b32 v230, v4, 10, v8
	v_lshlrev_b32_e32 v8, 2, v10
	v_lshlrev_b32_e32 v6, 1, v6
	v_or3_b32 v6, v8, v6, v12
	v_lshlrev_b32_e32 v8, 2, v3
	v_and_b32_e32 v10, 0xfffffc00, v8
	v_lshl_add_u32 v6, v6, 11, v10
	v_lshlrev_b32_e32 v10, 8, v11
	v_lshlrev_b32_e32 v9, 4, v9
	v_and_b32_e32 v15, 15, v3
	v_and_or_b32 v9, v9, 48, v10
	v_and_b32_e32 v10, 32, v16
	v_bitop3_b32 v220, v6, v9, v10 bitop3:0xf6
	v_lshlrev_b32_e32 v6, 6, v15
	v_and_b32_e32 v9, 48, v3
	v_and_b32_e32 v8, 32, v8
	v_or_b32_e32 v10, v6, v9
	v_bitop3_b32 v6, v6, v8, v9 bitop3:0x36
	v_lshlrev_b32_e32 v4, 13, v4
	v_ashrrev_i32_e32 v14, 8, v3
	v_and_or_b32 v227, v4, s66, v6
	v_lshlrev_b32_e32 v4, 16, v5
	v_lshlrev_b32_e32 v3, 10, v3
	s_mov_b32 s1, 0xf000
	v_lshlrev_b32_e32 v219, 6, v12
	v_and_or_b32 v3, v3, s1, v4
	v_lshlrev_b32_e32 v9, 14, v14
	v_lshl_or_b32 v225, v7, 1, v3
	v_cmp_eq_u32_e32 vcc, 0, v216
	v_add_u32_e32 v228, 0, v220
	v_add_u32_e32 v3, 0xc0, v219
	v_bitop3_b32 v217, v10, v9, v8 bitop3:0xde
	v_or_b32_e32 v218, 0x8000, v227
	v_readfirstlane_b32 s1, v14
	v_add_u32_e32 v226, 0x40000, v225
	v_add_u32_e32 v224, 0x80000, v225
	v_add_u32_e32 v223, 0xc0000, v225
	v_add_u32_e32 v229, v228, v219
	v_and_b32_e32 v221, 0xc0, v3
	s_mov_b64 s[6:7], s[10:11]
	s_cbranch_vccnz .LBB0_1574
; #define G_DMA_A(buf, t, i_) __builtin_amdgcn_raw_ptr_buffer_load_lds(ra, (LAS void*)(lds + (buf) * 65536 + a_wu + (i_) * 8192), 16, ao##i_, (unsigned)(t) * 128u, 0, 0)
; #define G_ISSUE_B(t) do { const unsigned so_ = (unsigned)(t) * 64u * ldbB; _Pragma("unroll") for (int i_ = 0; i_ < 8; ++i_) sb[i_] = __builtin_bit_cast(f32x4, __builtin_amdgcn_raw_buffer_load_b128(rb, bo, so_ + (unsigned)i_ * ldbB, 0)); } while (0)
; #define G_RETIRE() asm volatile("s_waitcnt vmcnt(0)" : "+v"(sb[0]), "+v"(sb[1]), "+v"(sb[2]), "+v"(sb[3]), "+v"(sb[4]), "+v"(sb[5]), "+v"(sb[6]), "+v"(sb[7]) :: "memory")
; #define G_WRITE_B(buf) do { LAS unsigned char* d_ = lds + (buf) * 65536; \
;         _Pragma("unroll") for (int j_ = 0; j_ < 4; ++j_) { u32x4 w_; w_.x = cvtpk(sb[0][j_], sb[1][j_]); w_.y = cvtpk(sb[2][j_], sb[3][j_]); w_.z = cvtpk(sb[4][j_], sb[5][j_]); w_.w = cvtpk(sb[6][j_], sb[7][j_]); \
;             *(LAS u32x4*)(d_ + 32768 + T.b_w + ((T.b_rot + 64u * j_) & 255u)) = w_; } } while (0)
; #define G_BAR() do { asm volatile("s_waitcnt lgkmcnt(0)" ::: "memory"); __builtin_amdgcn_s_barrier(); asm volatile("" ::: "memory"); } while (0)
; #define G_DMA_A(buf, t, i_) __builtin_amdgcn_raw_ptr_buffer_load_lds(ra, (LAS void*)(lds + (buf) * 65536 + a_wu + (i_) * 8192), 16, ao##i_, (unsigned)(t) * 128u, 0, 0)
; #define G_ISSUE_B(t) do { const unsigned so_ = (unsigned)(t) * 64u * ldbB; _Pragma("unroll") for (int i_ = 0; i_ < 8; ++i_) sb[i_] = __builtin_bit_cast(f32x4, __builtin_amdgcn_raw_buffer_load_b128(rb, bo, so_ + (unsigned)i_ * ldbB, 0)); } while (0)
; #define G_RETIRE() asm volatile("s_waitcnt vmcnt(0)" : "+v"(sb[0]), "+v"(sb[1]), "+v"(sb[2]), "+v"(sb[3]), "+v"(sb[4]), "+v"(sb[5]), "+v"(sb[6]), "+v"(sb[7]) :: "memory")
; __device__ __forceinline__ void gemm_kloop_light(f32x4 (&acc)[8][4], LAS unsigned char* lds, const GemmT& T, ...
;     ...
;     G_ISSUE_B(0); G_DMA_A(0, 0, 0); G_DMA_A(0, 0, 1); G_DMA_A(0, 0, 2); G_DMA_A(0, 0, 3); G_RETIRE(); G_WRITE_B(0);
;     if (nt > 1) G_ISSUE_B(1);
;     G_BAR();
; __device__ __forceinline__ void phase_moe_down(const Ptrs& p, LAS unsigned char* lds) {
;     ...
;         const int mlim = __builtin_amdgcn_readfirstlane(T.wr) ? 0 : ((mu.cnt - i0 + 15) >> 4);
;         if (mu.light) gemm_kloop_light(acc, lds, T, mk_rsrc(act + (size_t)(mu.base + i0) * D), ao, ao + 64u * 4096, ao + 128u * 4096, ao + 192u * 4096,
	s_sub_i32 s2, s83, s85
	s_add_i32 s2, s2, 15
	s_ashr_i32 s2, s2, 4
	s_cmp_eq_u32 s1, 0
	s_cselect_b32 s1, s2, 0
	v_readfirstlane_b32 s2, v230
	s_and_b32 s2, s2, 0xfffffc00
	s_add_i32 s2, s2, 0
	s_mov_b32 s38, s26
	s_mov_b32 s39, s27
	s_mov_b32 m0, s2
	s_waitcnt vmcnt(4)
	v_mov_b64_e32 v[4:5], v[118:119]
	buffer_load_dwordx4 v225, s[36:39], 0 offen lds
	s_add_i32 m0, s2, 0x2000
	s_waitcnt vmcnt(2)
	v_mov_b64_e32 v[8:9], v[138:139]
	buffer_load_dwordx4 v226, s[36:39], 0 offen lds
	s_add_i32 m0, s2, 0x4000
	v_mov_b64_e32 v[12:13], v[122:123]
	buffer_load_dwordx4 v224, s[36:39], 0 offen lds
	s_add_i32 m0, s2, 0x6000
	v_mov_b64_e32 v[16:17], v[114:115]
	v_mov_b64_e32 v[20:21], v[130:131]
	v_mov_b64_e32 v[24:25], v[110:111]
	s_waitcnt vmcnt(3)
	v_mov_b64_e32 v[28:29], v[142:143]
	v_mov_b64_e32 v[32:33], v[126:127]
	buffer_load_dwordx4 v223, s[36:39], 0 offen lds
	v_mov_b64_e32 v[6:7], v[120:121]
	v_mov_b64_e32 v[10:11], v[140:141]
	v_mov_b64_e32 v[14:15], v[124:125]
	v_mov_b64_e32 v[18:19], v[116:117]
	v_mov_b64_e32 v[22:23], v[132:133]
	v_mov_b64_e32 v[26:27], v[112:113]
	v_mov_b64_e32 v[30:31], v[144:145]
	v_mov_b64_e32 v[34:35], v[128:129]
	s_waitcnt vmcnt(0)
	buffer_load_dwordx4 v[162:165], v222, s[24:27], s67 offen
	buffer_load_dwordx4 v[170:173], v222, s[24:27], s68 offen
	buffer_load_dwordx4 v[174:177], v222, s[24:27], s69 offen
	buffer_load_dwordx4 v[178:181], v222, s[24:27], s70 offen
	buffer_load_dwordx4 v[182:185], v222, s[24:27], s71 offen
	buffer_load_dwordx4 v[186:189], v222, s[24:27], s76 offen
	buffer_load_dwordx4 v[190:193], v222, s[24:27], s77 offen
	buffer_load_dwordx4 v[194:197], v222, s[24:27], s78 offen
	s_cmp_gt_i32 s1, 0
	s_cselect_b64 s[60:61], -1, 0
	s_cmp_lg_u32 s1, 1
	v_cvt_pk_bf16_f32 v36, v24, v12
	v_cvt_pk_bf16_f32 v37, v32, v16
	v_cvt_pk_bf16_f32 v38, v4, v20
	v_cvt_pk_bf16_f32 v39, v8, v28
	s_cselect_b64 s[58:59], -1, 0
	s_cmp_gt_i32 s1, 2
	ds_write_b128 v229, v[36:39] offset:32768
	v_cvt_pk_bf16_f32 v36, v25, v13
	v_cvt_pk_bf16_f32 v37, v33, v17
	v_cvt_pk_bf16_f32 v38, v5, v21
	v_cvt_pk_bf16_f32 v39, v9, v29
	s_cselect_b64 s[54:55], -1, 0
	s_cmp_gt_i32 s1, 3
	ds_write_b128 v229, v[36:39] offset:32832
	v_cvt_pk_bf16_f32 v36, v26, v14
	v_cvt_pk_bf16_f32 v37, v34, v18
	v_cvt_pk_bf16_f32 v38, v6, v22
	v_cvt_pk_bf16_f32 v39, v10, v30
	v_cvt_pk_bf16_f32 v4, v27, v15
	v_cvt_pk_bf16_f32 v5, v35, v19
	v_cvt_pk_bf16_f32 v6, v7, v23
	v_cvt_pk_bf16_f32 v7, v11, v31
	v_add_u32_e32 v3, v228, v221
	s_cselect_b64 s[50:51], -1, 0
	s_cmp_gt_i32 s1, 4
	ds_write_b128 v229, v[36:39] offset:32896
	ds_write_b128 v3, v[4:7] offset:32768
	s_cselect_b64 s[48:49], -1, 0
	s_cmp_gt_i32 s1, 5
	s_waitcnt lgkmcnt(0)
	s_barrier
	s_cselect_b64 s[46:47], -1, 0
	s_cmp_gt_i32 s1, 6
	v_mov_b32_e32 v4, v2
	v_mov_b32_e32 v5, v2
	s_cselect_b64 s[44:45], -1, 0
	s_cmp_gt_i32 s1, 7
	v_mov_b32_e32 v3, v2
	v_mov_b64_e32 v[12:13], v[4:5]
	v_mov_b64_e32 v[8:9], v[4:5]
	v_mov_b64_e32 v[20:21], v[4:5]
	v_mov_b64_e32 v[16:17], v[4:5]
	v_mov_b64_e32 v[28:29], v[4:5]
	v_mov_b64_e32 v[24:25], v[4:5]
	v_mov_b64_e32 v[36:37], v[4:5]
	v_mov_b64_e32 v[32:33], v[4:5]
	v_mov_b64_e32 v[44:45], v[4:5]
	v_mov_b64_e32 v[40:41], v[4:5]
	v_mov_b64_e32 v[52:53], v[4:5]
	v_mov_b64_e32 v[48:49], v[4:5]
	v_mov_b64_e32 v[60:61], v[4:5]
	v_mov_b64_e32 v[56:57], v[4:5]
	v_mov_b64_e32 v[68:69], v[4:5]
	v_mov_b64_e32 v[64:65], v[4:5]
	v_mov_b64_e32 v[76:77], v[4:5]
	v_mov_b64_e32 v[72:73], v[4:5]
	v_mov_b64_e32 v[84:85], v[4:5]
	v_mov_b64_e32 v[80:81], v[4:5]
	v_mov_b64_e32 v[92:93], v[4:5]
	v_mov_b64_e32 v[88:89], v[4:5]
	v_mov_b64_e32 v[100:101], v[4:5]
	v_mov_b64_e32 v[96:97], v[4:5]
	v_mov_b64_e32 v[108:109], v[4:5]
	v_mov_b64_e32 v[104:105], v[4:5]
	v_mov_b64_e32 v[148:149], v[4:5]
	v_mov_b64_e32 v[136:137], v[4:5]
	v_mov_b64_e32 v[156:157], v[4:5]
	v_mov_b64_e32 v[152:153], v[4:5]
	v_mov_b64_e32 v[168:169], v[4:5]
	v_mov_b64_e32 v[160:161], v[4:5]
	s_mov_b32 s3, 0
	s_cselect_b64 s[34:35], -1, 0
	s_mov_b32 s72, 0x10e000
	s_movk_i32 s73, 0x80
	v_mov_b64_e32 v[10:11], v[2:3]
	v_mov_b64_e32 v[6:7], v[2:3]
	v_mov_b64_e32 v[18:19], v[2:3]
	v_mov_b64_e32 v[14:15], v[2:3]
	v_mov_b64_e32 v[26:27], v[2:3]
	v_mov_b64_e32 v[22:23], v[2:3]
	v_mov_b64_e32 v[34:35], v[2:3]
	v_mov_b64_e32 v[30:31], v[2:3]
	v_mov_b64_e32 v[42:43], v[2:3]
	v_mov_b64_e32 v[38:39], v[2:3]
	v_mov_b64_e32 v[50:51], v[2:3]
	v_mov_b64_e32 v[46:47], v[2:3]
	v_mov_b64_e32 v[58:59], v[2:3]
	v_mov_b64_e32 v[54:55], v[2:3]
	v_mov_b64_e32 v[66:67], v[2:3]
	v_mov_b64_e32 v[62:63], v[2:3]
	v_mov_b64_e32 v[74:75], v[2:3]
	v_mov_b64_e32 v[70:71], v[2:3]
	v_mov_b64_e32 v[82:83], v[2:3]
	v_mov_b64_e32 v[78:79], v[2:3]
	v_mov_b64_e32 v[90:91], v[2:3]
	v_mov_b64_e32 v[86:87], v[2:3]
	v_mov_b64_e32 v[98:99], v[2:3]
	v_mov_b64_e32 v[94:95], v[2:3]
	v_mov_b64_e32 v[106:107], v[2:3]
	v_mov_b64_e32 v[102:103], v[2:3]
	v_mov_b64_e32 v[146:147], v[2:3]
	v_mov_b64_e32 v[134:135], v[2:3]
	v_mov_b64_e32 v[154:155], v[2:3]
	v_mov_b64_e32 v[150:151], v[2:3]
	v_mov_b64_e32 v[166:167], v[2:3]
	v_mov_b64_e32 v[158:159], v[2:3]
	s_branch .LBB0_1486

; __device__ __forceinline__ float bflo(unsigned w) { return __uint_as_float(w << 16); }
; __device__ __forceinline__ float bfhi(unsigned w) { return __uint_as_float(w & 0xffff0000u); }
; __device__ __forceinline__ int vwg_id() { const int G = gridDim.x; return (G % 8 == 0) ? (int)((blockIdx.x % 8) * (G / 8) + blockIdx.x / 8) : (int)blockIdx.x; }
; __device__ __forceinline__ void phase_final(const Ptrs& p, LAS unsigned char* lds) {
;     ...
;     for (int row = vwg_id() * 8 + wid; row < NTOK; row += gridDim.x * 8) {
;         const int b = row / S; const float* gf = (const float*)(p.ws + OFF_MOD) + (size_t)b * NMOD + 5 * D; const float* xr = x1 + (size_t)row * D; const bf16_t* yr = y + (size_t)row * 4 * D;
;         f32x4 v[8]; float ss = 0.f;
; #pragma unroll
;         for (int c = 0; c < 8; ++c) { const int k = c * 256 + lane * 4; f32x4 s = {0.f, 0.f, 0.f, 0.f};
; #pragma unroll
;             for (int q = 0; q < 4; ++q) { const u32x2 w = __builtin_nontemporal_load((const u32x2*)(yr + (size_t)q * D + k)); s[0] += bflo(w.x); s[1] += bfhi(w.x); s[2] += bflo(w.y); s[3] += bfhi(w.y); }
;             v[c] = __builtin_nontemporal_load((const f32x4*)(xr + k)) + *(const f32x4*)(gf + k) * s; ss += v[c][0] * v[c][0] + v[c][1] * v[c][1] + v[c][2] * v[c][2] + v[c][3] * v[c][3]; }
.LBB0_1650:
	v_ashrrev_i32_e32 v1, 6, v0
	v_lshl_add_u32 v20, s94, 3, v1
	s_movk_i32 s4, 0x2000
	v_cmp_gt_i32_e32 vcc, s4, v20
	s_and_saveexec_b64 s[0:1], vcc
	s_cbranch_execz .LBB0_1653
	v_lshlrev_b32_e32 v0, 2, v0
	v_and_b32_e32 v0, 0xfc, v0
	v_mov_b32_e32 v23, 0
	v_or_b32_e32 v8, 0x400, v0
	v_lshlrev_b32_e32 v22, 2, v0
	v_or_b32_e32 v10, 0x500, v0
	v_lshl_add_u64 v[24:25], s[16:17], 0, v[22:23]
	v_lshlrev_b32_e32 v22, 2, v8
	v_or_b32_e32 v12, 0x600, v0
	v_lshl_add_u64 v[26:27], s[16:17], 0, v[22:23]
	v_lshlrev_b32_e32 v22, 2, v10
	v_or_b32_e32 v14, 0x700, v0
	v_lshl_add_u64 v[28:29], s[16:17], 0, v[22:23]
	v_lshlrev_b32_e32 v22, 2, v12
	v_lshl_add_u64 v[30:31], s[16:17], 0, v[22:23]
	v_lshlrev_b32_e32 v22, 2, v14
	v_or_b32_e32 v2, 0x100, v0
	v_or_b32_e32 v4, 0x200, v0
	v_or_b32_e32 v6, 0x300, v0
	v_lshl_add_u64 v[32:33], s[16:17], 0, v[22:23]
	v_lshlrev_b32_e32 v22, 1, v0
	s_lshl_b32 s5, s33, 3
	v_lshl_add_u64 v[34:35], s[22:23], 0, v[22:23]
	s_mov_b64 s[0:1], 0
	s_mov_b64 s[2:3], 0x1a000
	s_movk_i32 s6, 0x1000
	s_movk_i32 s7, 0x3000
	v_lshlrev_b32_e32 v22, 2, v0
	v_lshlrev_b32_e32 v36, 2, v2
	v_mov_b32_e32 v37, v23
	v_lshlrev_b32_e32 v38, 2, v4
	v_mov_b32_e32 v39, v23
	v_lshlrev_b32_e32 v40, 2, v6
	v_mov_b32_e32 v41, v23
	v_lshlrev_b32_e32 v42, 2, v8
	v_mov_b32_e32 v43, v23
	v_lshlrev_b32_e32 v44, 2, v10
	v_mov_b32_e32 v45, v23
	v_lshlrev_b32_e32 v46, 2, v12
	v_mov_b32_e32 v47, v23
	v_lshlrev_b32_e32 v48, 2, v14
	v_mov_b32_e32 v49, v23
	v_mov_b32_e32 v108, 0x358637bd
	s_mov_b32 s8, 0x800000
	s_movk_i32 s9, 0x1fff
	global_load_dwordx4 v[124:127], v[24:25], off offset:1024
	global_load_dwordx4 v[128:131], v[24:25], off offset:2048
	global_load_dwordx4 v[132:135], v[24:25], off offset:3072
	global_load_dwordx4 v[136:139], v[26:27], off
	global_load_dwordx4 v[140:143], v[28:29], off
	global_load_dwordx4 v[144:147], v[30:31], off
	global_load_dwordx4 v[148:151], v[32:33], off
	s_waitcnt vmcnt(0)
.LBB0_1652:
	v_ashrrev_i32_e32 v21, 31, v20
	v_lshlrev_b64 v[0:1], 14, v[20:21]
	v_lshl_add_u64 v[56:57], v[34:35], 0, v[0:1]
	v_add_co_u32_e32 v52, vcc, s4, v56
	v_lshrrev_b32_e32 v0, 20, v21
	s_nop 0
	v_addc_co_u32_e32 v53, vcc, 0, v57, vcc
	v_add_co_u32_e32 v60, vcc, s7, v56
	global_load_dwordx2 v[62:63], v[56:57], off nt
	s_nop 0
	v_addc_co_u32_e32 v61, vcc, 0, v57, vcc
	v_add_co_u32_e32 v82, vcc, s6, v56
	v_add_u32_e32 v0, v20, v0
	s_nop 0
	v_addc_co_u32_e32 v83, vcc, 0, v57, vcc
	v_ashrrev_i32_e32 v0, 12, v0
	global_load_dwordx2 v[64:65], v[56:57], off offset:512 nt
	global_load_dwordx2 v[76:77], v[52:53], off offset:-4096 nt
	global_load_dwordx2 v[74:75], v[52:53], off nt
	v_lshlrev_b64 v[50:51], 13, v[20:21]
	global_load_dwordx2 v[70:71], v[82:83], off offset:512 nt
	v_mul_hi_i32_i24_e32 v5, 0xc000, v0
	v_mul_i32_i24_e32 v4, 0xc000, v0
	global_load_dwordx2 v[78:79], v[60:61], off nt
	global_load_dwordx2 v[66:67], v[52:53], off offset:512 nt
	v_lshl_add_u64 v[54:55], s[40:41], 0, v[50:51]
	v_lshl_add_u64 v[4:5], s[30:31], 0, v[4:5]
	v_lshl_add_u64 v[68:69], v[54:55], 0, v[22:23]
	v_lshl_add_u64 v[58:59], v[4:5], 0, s[2:3]
	global_load_dwordx4 v[0:3], v[68:69], off nt
	v_lshl_add_u64 v[12:13], v[58:59], 0, v[22:23]
	global_load_dwordx4 v[4:7], v[12:13], off
	global_load_dwordx2 v[72:73], v[60:61], off offset:512 nt
	global_load_dwordx4 v[8:11], v[68:69], off offset:1024 nt
	v_lshl_add_u64 v[106:107], v[58:59], 0, v[36:37]
	global_load_dwordx4 v[12:15], v[106:107], off
	global_load_dwordx2 v[80:81], v[56:57], off offset:1024 nt
	global_load_dwordx2 v[90:91], v[56:57], off offset:1536 nt
	global_load_dwordx2 v[104:105], v[82:83], off offset:1024 nt
	global_load_dwordx2 v[102:103], v[52:53], off offset:1024 nt
	global_load_dwordx4 v[16:19], v[68:69], off offset:2048 nt
	global_load_dwordx2 v[88:89], v[52:53], off offset:1536 nt
	global_load_dwordx2 v[100:101], v[60:61], off offset:1024 nt
	global_load_dwordx2 v[84:85], v[60:61], off offset:1536 nt
	global_load_dwordx2 v[94:95], v[82:83], off offset:1536 nt
	global_load_dwordx2 v[96:97], v[82:83], off offset:2048 nt
	global_load_dwordx2 v[92:93], v[82:83], off offset:2560 nt
	global_load_dwordx2 v[86:87], v[82:83], off offset:3072 nt
	global_load_dwordx2 v[98:99], v[82:83], off offset:3584 nt
	v_lshl_add_u64 v[82:83], v[58:59], 0, v[38:39]
	global_load_dwordx4 v[110:113], v[82:83], off
	v_lshl_add_u64 v[50:51], s[18:19], 0, v[50:51]
	v_add_u32_e32 v20, s5, v20
	s_waitcnt vmcnt(25)
	v_lshlrev_b32_e32 v82, 16, v62
	v_and_b32_e32 v83, 0xffff0000, v62
	v_lshlrev_b32_e32 v62, 16, v63
	v_and_b32_e32 v63, 0xffff0000, v63
	v_pk_add_f32 v[82:83], v[82:83], 0 op_sel_hi:[1,0]
	v_pk_add_f32 v[62:63], v[62:63], 0 op_sel_hi:[1,0]
	s_waitcnt vmcnt(24)
	v_lshlrev_b32_e32 v106, 16, v64
	v_and_b32_e32 v107, 0xffff0000, v64
	s_waitcnt vmcnt(23)
	v_lshlrev_b32_e32 v114, 16, v76
	v_and_b32_e32 v115, 0xffff0000, v76
	s_waitcnt vmcnt(22)
	v_lshlrev_b32_e32 v116, 16, v74
	v_and_b32_e32 v117, 0xffff0000, v74
	v_lshlrev_b32_e32 v76, 16, v77
	v_and_b32_e32 v77, 0xffff0000, v77
	v_pk_add_f32 v[106:107], v[106:107], 0 op_sel_hi:[1,0]
	s_waitcnt vmcnt(21)
	v_lshlrev_b32_e32 v120, 16, v70
	v_and_b32_e32 v121, 0xffff0000, v70
	v_pk_add_f32 v[82:83], v[82:83], v[114:115]
	s_waitcnt vmcnt(20)
	v_lshlrev_b32_e32 v118, 16, v78
	v_and_b32_e32 v119, 0xffff0000, v78
	v_lshlrev_b32_e32 v74, 16, v75
	v_and_b32_e32 v75, 0xffff0000, v75
	s_waitcnt vmcnt(19)
	v_lshlrev_b32_e32 v122, 16, v66
	v_and_b32_e32 v123, 0xffff0000, v66
	v_pk_add_f32 v[62:63], v[62:63], v[76:77]
	v_pk_add_f32 v[76:77], v[106:107], v[120:121]
	v_pk_add_f32 v[82:83], v[82:83], v[116:117]
	v_lshlrev_b32_e32 v78, 16, v79
	v_and_b32_e32 v79, 0xffff0000, v79
	v_pk_add_f32 v[62:63], v[62:63], v[74:75]
	v_pk_add_f32 v[74:75], v[76:77], v[122:123]
	v_pk_add_f32 v[76:77], v[82:83], v[118:119]
	v_pk_add_f32 v[62:63], v[62:63], v[78:79]
	s_waitcnt vmcnt(17)
; __device__ __forceinline__ float bflo(unsigned w) { return __uint_as_float(w << 16); }
; __device__ __forceinline__ float bfhi(unsigned w) { return __uint_as_float(w & 0xffff0000u); }
; __device__ __forceinline__ void phase_final(const Ptrs& p, LAS unsigned char* lds) {
;     ...
;         for (int c = 0; c < 8; ++c) { const int k = c * 256 + lane * 4; f32x4 s = {0.f, 0.f, 0.f, 0.f};
; #pragma unroll
;             for (int q = 0; q < 4; ++q) { const u32x2 w = __builtin_nontemporal_load((const u32x2*)(yr + (size_t)q * D + k)); s[0] += bflo(w.x); s[1] += bfhi(w.x); s[2] += bflo(w.y); s[3] += bfhi(w.y); }
;             v[c] = __builtin_nontemporal_load((const f32x4*)(xr + k)) + *(const f32x4*)(gf + k) * s; ss += v[c][0] * v[c][0] + v[c][1] * v[c][1] + v[c][2] * v[c][2] + v[c][3] * v[c][3]; }
	v_pk_fma_f32 v[0:1], v[4:5], v[76:77], v[0:1]
	s_waitcnt vmcnt(16)
	v_lshlrev_b32_e32 v4, 16, v72
	v_and_b32_e32 v5, 0xffff0000, v72
	v_pk_fma_f32 v[2:3], v[6:7], v[62:63], v[2:3]
	v_pk_add_f32 v[6:7], v[74:75], v[4:5]
	v_lshlrev_b32_e32 v4, 16, v65
	v_and_b32_e32 v5, 0xffff0000, v65
	v_pk_add_f32 v[4:5], v[4:5], 0 op_sel_hi:[1,0]
	v_lshlrev_b32_e32 v62, 16, v71
	v_and_b32_e32 v63, 0xffff0000, v71
	v_pk_add_f32 v[4:5], v[4:5], v[62:63]
	v_lshlrev_b32_e32 v62, 16, v67
	v_and_b32_e32 v63, 0xffff0000, v67
	v_lshl_add_u64 v[66:67], v[58:59], 0, v[40:41]
	v_pk_add_f32 v[4:5], v[4:5], v[62:63]
	global_load_dwordx4 v[62:65], v[68:69], off offset:3072 nt
	global_load_dwordx2 v[82:83], v[60:61], off offset:2048 nt
	global_load_dwordx2 v[106:107], v[56:57], off offset:2048 nt
	global_load_dwordx2 v[114:115], v[52:53], off offset:2048 nt
	v_lshlrev_b32_e32 v70, 16, v73
	global_load_dwordx4 v[66:69], v[66:67], off
	v_and_b32_e32 v71, 0xffff0000, v73
	s_waitcnt vmcnt(19)
	v_pk_fma_f32 v[6:7], v[12:13], v[6:7], v[8:9]
	v_mul_f32_e32 v21, v1, v1
	v_pk_add_f32 v[4:5], v[4:5], v[70:71]
	v_mul_f32_e32 v8, v7, v7
	v_fmac_f32_e32 v21, v0, v0
	v_pk_fma_f32 v[4:5], v[14:15], v[4:5], v[10:11]
	v_fmac_f32_e32 v8, v6, v6
	v_fmac_f32_e32 v21, v2, v2
	v_fmac_f32_e32 v8, v4, v4
	v_fmac_f32_e32 v21, v3, v3
	v_fmac_f32_e32 v8, v5, v5
	v_add_f32_e32 v21, v21, v8
	s_waitcnt vmcnt(18)
	v_lshlrev_b32_e32 v8, 16, v80
	v_and_b32_e32 v9, 0xffff0000, v80
	v_pk_add_f32 v[8:9], v[8:9], 0 op_sel_hi:[1,0]
	s_waitcnt vmcnt(16)
	v_lshlrev_b32_e32 v10, 16, v104
	v_and_b32_e32 v11, 0xffff0000, v104
	v_lshl_add_u64 v[14:15], v[54:55], 0, v[42:43]
	v_pk_add_f32 v[8:9], v[8:9], v[10:11]
	s_waitcnt vmcnt(15)
	v_lshlrev_b32_e32 v10, 16, v102
	v_and_b32_e32 v11, 0xffff0000, v102
	v_lshl_add_u64 v[78:79], v[58:59], 0, v[42:43]
	global_load_dwordx4 v[70:73], v[14:15], off nt
	global_load_dwordx4 v[74:77], v[78:79], off
	v_pk_add_f32 v[8:9], v[8:9], v[10:11]
	s_waitcnt vmcnt(14)
	v_lshlrev_b32_e32 v10, 16, v100
	v_and_b32_e32 v11, 0xffff0000, v100
	v_pk_add_f32 v[10:11], v[8:9], v[10:11]
	v_lshlrev_b32_e32 v8, 16, v81
	v_and_b32_e32 v9, 0xffff0000, v81
	v_pk_add_f32 v[8:9], v[8:9], 0 op_sel_hi:[1,0]
	v_lshlrev_b32_e32 v12, 16, v105
	v_and_b32_e32 v13, 0xffff0000, v105
	v_pk_add_f32 v[8:9], v[8:9], v[12:13]
	v_lshlrev_b32_e32 v12, 16, v103
	v_and_b32_e32 v13, 0xffff0000, v103
	v_pk_add_f32 v[8:9], v[8:9], v[12:13]
	v_lshlrev_b32_e32 v12, 16, v101
	v_and_b32_e32 v13, 0xffff0000, v101
	global_load_dwordx2 v[100:101], v[56:57], off offset:2560 nt
	global_load_dwordx2 v[102:103], v[52:53], off offset:2560 nt
	s_waitcnt vmcnt(9)
	v_pk_fma_f32 v[10:11], v[110:111], v[10:11], v[16:17]
	v_pk_add_f32 v[8:9], v[8:9], v[12:13]
	v_mul_f32_e32 v12, v11, v11
	v_pk_fma_f32 v[8:9], v[112:113], v[8:9], v[18:19]
	v_fmac_f32_e32 v12, v10, v10
	v_fmac_f32_e32 v12, v8, v8
	v_fmac_f32_e32 v12, v9, v9
	v_add_f32_e32 v21, v21, v12
	v_lshlrev_b32_e32 v12, 16, v90
	v_and_b32_e32 v13, 0xffff0000, v90
	v_pk_add_f32 v[12:13], v[12:13], 0 op_sel_hi:[1,0]
	v_lshlrev_b32_e32 v14, 16, v94
	v_and_b32_e32 v15, 0xffff0000, v94
	v_pk_add_f32 v[12:13], v[12:13], v[14:15]
	v_lshlrev_b32_e32 v14, 16, v88
	v_and_b32_e32 v15, 0xffff0000, v88
	global_load_dwordx2 v[110:111], v[60:61], off offset:2560 nt
	global_load_dwordx2 v[104:105], v[52:53], off offset:3072 nt
	v_pk_add_f32 v[12:13], v[12:13], v[14:15]
	v_lshlrev_b32_e32 v14, 16, v84
	v_and_b32_e32 v15, 0xffff0000, v84
	v_pk_add_f32 v[14:15], v[12:13], v[14:15]
	v_lshlrev_b32_e32 v12, 16, v91
	v_and_b32_e32 v13, 0xffff0000, v91
	v_pk_add_f32 v[12:13], v[12:13], 0 op_sel_hi:[1,0]
	v_lshlrev_b32_e32 v16, 16, v95
	v_and_b32_e32 v17, 0xffff0000, v95
	v_lshl_add_u64 v[18:19], v[54:55], 0, v[44:45]
	v_pk_add_f32 v[12:13], v[12:13], v[16:17]
	v_lshlrev_b32_e32 v16, 16, v89
	v_and_b32_e32 v17, 0xffff0000, v89
	v_lshl_add_u64 v[94:95], v[58:59], 0, v[44:45]
	global_load_dwordx4 v[78:81], v[18:19], off nt
	global_load_dwordx4 v[88:91], v[94:95], off
	v_pk_add_f32 v[12:13], v[12:13], v[16:17]
	v_lshlrev_b32_e32 v16, 16, v85
	v_and_b32_e32 v17, 0xffff0000, v85
	global_load_dwordx2 v[84:85], v[56:57], off offset:3072 nt
	global_load_dwordx2 v[94:95], v[56:57], off offset:3584 nt
	global_load_dwordx2 v[112:113], v[60:61], off offset:3072 nt
	s_waitcnt vmcnt(11)
	v_pk_fma_f32 v[14:15], v[66:67], v[14:15], v[62:63]
	v_pk_add_f32 v[12:13], v[12:13], v[16:17]
	v_mul_f32_e32 v16, v15, v15
	v_pk_fma_f32 v[12:13], v[68:69], v[12:13], v[64:65]
	v_fmac_f32_e32 v16, v14, v14
	v_fmac_f32_e32 v16, v12, v12
	v_fmac_f32_e32 v16, v13, v13
	v_add_f32_e32 v21, v21, v16
	v_lshlrev_b32_e32 v16, 16, v106
	v_and_b32_e32 v17, 0xffff0000, v106
	v_pk_add_f32 v[16:17], v[16:17], 0 op_sel_hi:[1,0]
	v_lshlrev_b32_e32 v18, 16, v96
	v_and_b32_e32 v19, 0xffff0000, v96
	v_pk_add_f32 v[16:17], v[16:17], v[18:19]
	v_lshlrev_b32_e32 v18, 16, v114
	v_and_b32_e32 v19, 0xffff0000, v114
	v_pk_add_f32 v[16:17], v[16:17], v[18:19]
	v_lshlrev_b32_e32 v18, 16, v82
	v_and_b32_e32 v19, 0xffff0000, v82
	v_lshl_add_u64 v[56:57], v[54:55], 0, v[46:47]
	v_pk_add_f32 v[18:19], v[16:17], v[18:19]
	v_lshlrev_b32_e32 v16, 16, v107
	v_and_b32_e32 v17, 0xffff0000, v107
	v_lshl_add_u64 v[106:107], v[58:59], 0, v[46:47]
	global_load_dwordx4 v[62:65], v[56:57], off nt
	global_load_dwordx4 v[66:69], v[106:107], off
	v_pk_add_f32 v[16:17], v[16:17], 0 op_sel_hi:[1,0]
	v_lshlrev_b32_e32 v56, 16, v97
	v_and_b32_e32 v57, 0xffff0000, v97
	v_pk_add_f32 v[16:17], v[16:17], v[56:57]
	v_lshlrev_b32_e32 v56, 16, v115
	v_and_b32_e32 v57, 0xffff0000, v115
	v_pk_add_f32 v[16:17], v[16:17], v[56:57]
	v_lshlrev_b32_e32 v56, 16, v83
	v_and_b32_e32 v57, 0xffff0000, v83
	s_waitcnt vmcnt(11)
; __device__ __forceinline__ float bflo(unsigned w) { return __uint_as_float(w << 16); }
; __device__ __forceinline__ float bfhi(unsigned w) { return __uint_as_float(w & 0xffff0000u); }
; __device__ __forceinline__ void phase_final(const Ptrs& p, LAS unsigned char* lds) {
;     ...
;         for (int c = 0; c < 8; ++c) { const int k = c * 256 + lane * 4; f32x4 s = {0.f, 0.f, 0.f, 0.f};
; #pragma unroll
;             for (int q = 0; q < 4; ++q) { const u32x2 w = __builtin_nontemporal_load((const u32x2*)(yr + (size_t)q * D + k)); s[0] += bflo(w.x); s[1] += bfhi(w.x); s[2] += bflo(w.y); s[3] += bfhi(w.y); }
;             v[c] = __builtin_nontemporal_load((const f32x4*)(xr + k)) + *(const f32x4*)(gf + k) * s; ss += v[c][0] * v[c][0] + v[c][1] * v[c][1] + v[c][2] * v[c][2] + v[c][3] * v[c][3]; }
	v_pk_fma_f32 v[18:19], v[74:75], v[18:19], v[70:71]
	v_pk_add_f32 v[16:17], v[16:17], v[56:57]
	global_load_dwordx2 v[74:75], v[52:53], off offset:3584 nt
	v_pk_fma_f32 v[16:17], v[76:77], v[16:17], v[72:73]
	global_load_dwordx2 v[60:61], v[60:61], off offset:3584 nt
	v_mul_f32_e32 v52, v19, v19
	v_fmac_f32_e32 v52, v18, v18
	v_fmac_f32_e32 v52, v16, v16
	v_fmac_f32_e32 v52, v17, v17
	v_add_f32_e32 v21, v21, v52
	s_waitcnt vmcnt(12)
	v_lshlrev_b32_e32 v52, 16, v100
	v_and_b32_e32 v53, 0xffff0000, v100
	v_pk_add_f32 v[52:53], v[52:53], 0 op_sel_hi:[1,0]
	v_lshlrev_b32_e32 v56, 16, v92
	v_and_b32_e32 v57, 0xffff0000, v92
	v_lshl_add_u64 v[76:77], v[54:55], 0, v[48:49]
	v_pk_add_f32 v[70:71], v[52:53], v[56:57]
	v_lshl_add_u64 v[82:83], v[58:59], 0, v[48:49]
	global_load_dwordx4 v[52:55], v[76:77], off nt
	global_load_dwordx4 v[56:59], v[82:83], off
	s_waitcnt vmcnt(13)
	v_lshlrev_b32_e32 v72, 16, v102
	v_and_b32_e32 v73, 0xffff0000, v102
	v_pk_add_f32 v[70:71], v[70:71], v[72:73]
	v_lshlrev_b32_e32 v76, 16, v93
	s_waitcnt vmcnt(12)
	v_lshlrev_b32_e32 v72, 16, v110
	v_and_b32_e32 v73, 0xffff0000, v110
	v_pk_add_f32 v[70:71], v[70:71], v[72:73]
	v_lshlrev_b32_e32 v72, 16, v101
	v_and_b32_e32 v73, 0xffff0000, v101
	v_pk_add_f32 v[72:73], v[72:73], 0 op_sel_hi:[1,0]
	v_and_b32_e32 v77, 0xffff0000, v93
	v_pk_add_f32 v[72:73], v[72:73], v[76:77]
	v_lshlrev_b32_e32 v76, 16, v103
	v_and_b32_e32 v77, 0xffff0000, v103
	v_pk_add_f32 v[72:73], v[72:73], v[76:77]
	v_lshlrev_b32_e32 v76, 16, v111
	v_and_b32_e32 v77, 0xffff0000, v111
	v_pk_add_f32 v[72:73], v[72:73], v[76:77]
	s_waitcnt vmcnt(11)
	v_lshlrev_b32_e32 v82, 16, v104
	v_and_b32_e32 v83, 0xffff0000, v104
	s_waitcnt vmcnt(9)
	v_pk_fma_f32 v[78:79], v[88:89], v[70:71], v[78:79]
	v_pk_fma_f32 v[76:77], v[90:91], v[72:73], v[80:81]
	v_mul_f32_e32 v70, v79, v79
	v_fmac_f32_e32 v70, v78, v78
	v_fmac_f32_e32 v70, v76, v76
	v_fmac_f32_e32 v70, v77, v77
	v_add_f32_e32 v21, v21, v70
	s_waitcnt vmcnt(8)
	v_lshlrev_b32_e32 v70, 16, v84
	v_and_b32_e32 v71, 0xffff0000, v84
	v_pk_add_f32 v[70:71], v[70:71], 0 op_sel_hi:[1,0]
	v_lshlrev_b32_e32 v72, 16, v86
	v_and_b32_e32 v73, 0xffff0000, v86
	v_pk_add_f32 v[80:81], v[70:71], v[72:73]
	global_load_dwordx4 v[70:73], v[24:25], off
	v_pk_add_f32 v[80:81], v[80:81], v[82:83]
	s_waitcnt vmcnt(7)
	v_lshlrev_b32_e32 v82, 16, v112
	v_and_b32_e32 v83, 0xffff0000, v112
	v_pk_add_f32 v[80:81], v[80:81], v[82:83]
	v_lshlrev_b32_e32 v82, 16, v85
	v_and_b32_e32 v83, 0xffff0000, v85
	v_pk_add_f32 v[82:83], v[82:83], 0 op_sel_hi:[1,0]
	v_lshlrev_b32_e32 v84, 16, v87
	v_and_b32_e32 v85, 0xffff0000, v87
	v_pk_add_f32 v[82:83], v[82:83], v[84:85]
	v_lshlrev_b32_e32 v84, 16, v105
	v_and_b32_e32 v85, 0xffff0000, v105
	v_pk_add_f32 v[82:83], v[82:83], v[84:85]
	v_lshlrev_b32_e32 v84, 16, v113
	v_and_b32_e32 v85, 0xffff0000, v113
	v_pk_add_f32 v[82:83], v[82:83], v[84:85]
	s_waitcnt vmcnt(5)
	v_pk_fma_f32 v[62:63], v[66:67], v[80:81], v[62:63]
	s_nop 0
	v_mul_f32_e32 v66, v63, v63
	v_pk_fma_f32 v[64:65], v[68:69], v[82:83], v[64:65]
	v_fmac_f32_e32 v66, v62, v62
	v_fmac_f32_e32 v66, v64, v64
	v_fmac_f32_e32 v66, v65, v65
	v_add_f32_e32 v21, v21, v66
	v_lshlrev_b32_e32 v66, 16, v94
	v_and_b32_e32 v67, 0xffff0000, v94
	v_pk_add_f32 v[66:67], v[66:67], 0 op_sel_hi:[1,0]
	v_lshlrev_b32_e32 v68, 16, v98
	v_and_b32_e32 v69, 0xffff0000, v98
	v_pk_add_f32 v[66:67], v[66:67], v[68:69]
	s_waitcnt vmcnt(4)
	v_lshlrev_b32_e32 v68, 16, v74
	v_and_b32_e32 v69, 0xffff0000, v74
	v_pk_add_f32 v[66:67], v[66:67], v[68:69]
	s_waitcnt vmcnt(3)
; template <int CTRL> __device__ __forceinline__ float dppf(float x) { return __builtin_bit_cast(float, __builtin_amdgcn_mov_dpp(__builtin_bit_cast(int, x), CTRL, 0xf, 0xf, true)); }
; __device__ __forceinline__ float xrow_sum(float x) { const auto s = __builtin_amdgcn_permlane16_swap(__float_as_uint(x), __float_as_uint(x), false, false); x = __uint_as_float(s[0]) + __uint_as_float(s[1]); return xhalf_sum(x); }
; __device__ __forceinline__ float wave_sum(float v) { v += dppf<DPP_XOR1>(v); v += dppf<DPP_XOR2>(v); v += dppf<DPP_XOR7>(v); v += dppf<DPP_XOR8>(v); return xrow_sum(v); }
; __device__ __forceinline__ void phase_final(const Ptrs& p, LAS unsigned char* lds) {
;     ...
;         ss = wave_sum(ss); const float r = rsqrtf(ss * (1.0f / D) + EPS);
; #pragma unroll
;         for (int c = 0; c < 8; ++c) { const int k = c * 256 + lane * 4; __builtin_nontemporal_store((v[c] * r) * *(const f32x4*)(p.final_g + k), (f32x4*)(p.out + (size_t)row * D + k)); }
	v_lshlrev_b32_e32 v68, 16, v60
	v_and_b32_e32 v69, 0xffff0000, v60
	v_pk_add_f32 v[66:67], v[66:67], v[68:69]
	v_lshlrev_b32_e32 v68, 16, v95
	v_and_b32_e32 v69, 0xffff0000, v95
	v_pk_add_f32 v[68:69], v[68:69], 0 op_sel_hi:[1,0]
	v_lshlrev_b32_e32 v80, 16, v99
	v_and_b32_e32 v81, 0xffff0000, v99
	v_pk_add_f32 v[68:69], v[68:69], v[80:81]
	v_lshlrev_b32_e32 v74, 16, v75
	v_and_b32_e32 v75, 0xffff0000, v75
	v_pk_add_f32 v[68:69], v[68:69], v[74:75]
	v_lshlrev_b32_e32 v60, 16, v61
	v_and_b32_e32 v61, 0xffff0000, v61
	s_waitcnt vmcnt(1)
	v_pk_fma_f32 v[52:53], v[56:57], v[66:67], v[52:53]
	v_pk_add_f32 v[60:61], v[68:69], v[60:61]
	v_mul_f32_e32 v56, v53, v53
	v_pk_fma_f32 v[54:55], v[58:59], v[60:61], v[54:55]
	v_fmac_f32_e32 v56, v52, v52
	v_fmac_f32_e32 v56, v54, v54
	v_fmac_f32_e32 v56, v55, v55
	v_add_f32_e32 v21, v21, v56
	v_lshl_add_u64 v[58:59], v[50:51], 0, v[22:23]
	s_nop 0
	v_add_f32_dpp v21, v21, v21 quad_perm:[1,0,3,2] row_mask:0xf bank_mask:0xf bound_ctrl:1
	s_nop 1
	v_add_f32_dpp v21, v21, v21 quad_perm:[2,3,0,1] row_mask:0xf bank_mask:0xf bound_ctrl:1
	s_nop 1
	v_add_f32_dpp v21, v21, v21 row_half_mirror row_mask:0xf bank_mask:0xf bound_ctrl:1
	s_nop 1
	v_add_f32_dpp v21, v21, v21 row_ror:8 row_mask:0xf bank_mask:0xf bound_ctrl:1
	v_mov_b32_e32 v56, v21
	s_nop 1
	v_permlane16_swap_b32_e32 v21, v56
	v_add_f32_e32 v21, v21, v56
	v_mov_b32_e32 v56, v21
	s_nop 1
	v_permlane32_swap_b32_e32 v21, v56
	v_add_f32_e32 v21, v21, v56
	v_fmamk_f32 v21, v21, 0x3a000000, v108
	v_mul_f32_e32 v56, 0x4b800000, v21
	v_cmp_gt_f32_e32 vcc, s8, v21
	s_nop 1
	v_cndmask_b32_e32 v21, v21, v56, vcc
	v_rsq_f32_e32 v21, v21
	s_nop 0
	v_mul_f32_e32 v56, 0x45800000, v21
	v_cndmask_b32_e32 v56, v21, v56, vcc
	v_pk_mul_f32 v[0:1], v[0:1], v[56:57] op_sel_hi:[1,0]
	v_pk_mul_f32 v[2:3], v[2:3], v[56:57] op_sel_hi:[1,0]
	s_waitcnt vmcnt(0)
	v_pk_mul_f32 v[0:1], v[70:71], v[0:1]
	v_pk_mul_f32 v[2:3], v[72:73], v[2:3]
	global_store_dwordx4 v[58:59], v[0:3], off nt
	s_nop 1
	v_pk_mul_f32 v[4:5], v[4:5], v[56:57] op_sel_hi:[1,0]
	v_pk_mul_f32 v[6:7], v[6:7], v[56:57] op_sel_hi:[1,0]
	v_cmp_lt_i32_e32 vcc, s9, v20
	s_or_b64 s[0:1], vcc, s[0:1]
	v_pk_mul_f32 v[0:1], v[124:125], v[6:7]
	v_pk_mul_f32 v[2:3], v[126:127], v[4:5]
	global_store_dwordx4 v[58:59], v[0:3], off offset:1024 nt
	s_nop 1
	v_pk_mul_f32 v[4:5], v[8:9], v[56:57] op_sel_hi:[1,0]
	v_pk_mul_f32 v[6:7], v[10:11], v[56:57] op_sel_hi:[1,0]
	v_pk_mul_f32 v[8:9], v[18:19], v[56:57] op_sel_hi:[1,0]
	v_pk_mul_f32 v[0:1], v[128:129], v[6:7]
	v_pk_mul_f32 v[2:3], v[130:131], v[4:5]
	global_store_dwordx4 v[58:59], v[0:3], off offset:2048 nt
	s_nop 1
	v_pk_mul_f32 v[4:5], v[12:13], v[56:57] op_sel_hi:[1,0]
	v_pk_mul_f32 v[6:7], v[14:15], v[56:57] op_sel_hi:[1,0]
	v_pk_mul_f32 v[2:3], v[134:135], v[4:5]
	v_pk_mul_f32 v[0:1], v[132:133], v[6:7]
	global_store_dwordx4 v[58:59], v[0:3], off offset:3072 nt
	s_nop 1
	v_pk_mul_f32 v[6:7], v[16:17], v[56:57] op_sel_hi:[1,0]
	v_lshl_add_u64 v[4:5], v[50:51], 0, v[42:43]
	v_pk_mul_f32 v[0:1], v[136:137], v[8:9]
	v_pk_mul_f32 v[2:3], v[138:139], v[6:7]
	global_store_dwordx4 v[4:5], v[0:3], off nt
	s_nop 1
	v_pk_mul_f32 v[6:7], v[76:77], v[56:57] op_sel_hi:[1,0]
	v_pk_mul_f32 v[8:9], v[78:79], v[56:57] op_sel_hi:[1,0]
	v_lshl_add_u64 v[4:5], v[50:51], 0, v[44:45]
	v_pk_mul_f32 v[0:1], v[140:141], v[8:9]
	v_pk_mul_f32 v[2:3], v[142:143], v[6:7]
	global_store_dwordx4 v[4:5], v[0:3], off nt
	s_nop 1
	v_pk_mul_f32 v[6:7], v[64:65], v[56:57] op_sel_hi:[1,0]
	v_pk_mul_f32 v[8:9], v[62:63], v[56:57] op_sel_hi:[1,0]
	v_lshl_add_u64 v[4:5], v[50:51], 0, v[46:47]
	v_pk_mul_f32 v[0:1], v[8:9], v[144:145]
	v_pk_mul_f32 v[2:3], v[6:7], v[146:147]
	global_store_dwordx4 v[4:5], v[0:3], off nt
	s_nop 1
	v_pk_mul_f32 v[6:7], v[54:55], v[56:57] op_sel_hi:[1,0]
	v_pk_mul_f32 v[8:9], v[52:53], v[56:57] op_sel_hi:[1,0]
	v_lshl_add_u64 v[4:5], v[50:51], 0, v[48:49]
	v_pk_mul_f32 v[0:1], v[8:9], v[148:149]
	v_pk_mul_f32 v[2:3], v[6:7], v[150:151]
	global_store_dwordx4 v[4:5], v[0:3], off nt
	s_nop 1
	s_andn2_b64 exec, exec, s[0:1]
	s_cbranch_execnz .LBB0_1652
